# move 2048 layer-1 down-proj weight conversion items from the prologue into the idle half round at the end of the in-proj phase (WGs 128-255, one item per wave per layer)
# speedup vs baseline: 1.0216x; 1.0216x over previous
.LBB0_41:
	v_writelane_b32 v253, s24, 32
	v_writelane_b32 v253, s23, 34
	v_writelane_b32 v253, s22, 36
	s_mov_b32 s3, 0
	v_readlane_b32 s0, v253, 29
	s_lshl_b32 s0, s0, 14
	s_add_i32 s29, s0, 0
	s_cmp_lg_u64 s[48:49], 0
	v_readlane_b32 s4, v253, 30
	s_cselect_b64 s[44:45], -1, 0
	s_abs_i32 s2, s4
	v_cvt_f32_u32_e32 v2, s2
	s_sub_i32 s0, 0, s2
	s_ashr_i32 s6, s4, 31
	v_rcp_iflag_f32_e32 v2, v2
	s_nop 0
	v_mul_f32_e32 v2, 0x4f7ffffe, v2
	v_cvt_u32_f32_e32 v2, v2
	s_nop 0
	v_readfirstlane_b32 s1, v2
	s_mul_i32 s0, s0, s1
	s_mul_hi_u32 s0, s1, s0
	s_add_i32 s7, s1, s0
	s_mul_hi_u32 s0, s7, 0x4200
	s_mul_i32 s0, s0, s2
	s_sub_i32 s0, 0x4200, s0
	s_sub_i32 s1, s0, s2
	s_cmp_ge_u32 s0, s2
	s_cselect_b32 s0, s1, s0
	s_sub_i32 s1, s0, s2
	s_cmp_ge_u32 s0, s2
	s_cselect_b32 s8, s1, s0
	s_add_i32 s0, s4, 0xffffff00
	s_cmp_ge_i32 s0, s8
	s_cselect_b64 s[0:1], -1, 0
	s_cmpk_lt_u32 s8, 0x2101
	s_cselect_b64 s[4:5], -1, 0
	s_sub_i32 s8, 0x4200, s8
	s_and_b64 s[0:1], s[0:1], s[4:5]
	s_and_b64 s[0:1], s[0:1], exec
	s_cselect_b32 s5, s8, 0x4200
	s_add_i32 s0, s5, 0xfffff800
	s_cmp_eq_u32 s2, 0x800
	s_cselect_b32 s5, s0, s5
	v_writelane_b32 v253, s5, 38
	v_writelane_b32 v253, s48, 40
	s_mul_hi_u32 s0, s5, s7
	s_mul_i32 s1, s0, s2
	v_writelane_b32 v253, s49, 41
	v_writelane_b32 v253, s50, 42
	v_writelane_b32 v253, s51, 43
	v_writelane_b32 v253, s52, 44
	v_writelane_b32 v253, s53, 45
	v_writelane_b32 v253, s54, 46
	v_writelane_b32 v253, s55, 47
	s_sub_i32 s1, s5, s1
	v_writelane_b32 v253, s56, 48
	s_add_i32 s4, s0, 1
	s_sub_i32 s5, s1, s2
	v_writelane_b32 v253, s57, 49
	s_cmp_ge_u32 s1, s2
	v_writelane_b32 v253, s58, 50
	s_cselect_b32 s0, s4, s0
	v_writelane_b32 v253, s59, 51
	s_cselect_b32 s1, s5, s1
	s_add_i32 s4, s0, 1
	v_writelane_b32 v253, s60, 52
	s_cmp_ge_u32 s1, s2
	v_writelane_b32 v253, s61, 53
	s_cselect_b32 s0, s4, s0
	v_writelane_b32 v253, s62, 54
	s_xor_b32 s0, s0, s6
	v_writelane_b32 v253, s63, 55
	s_sub_i32 s15, s0, s6
	v_writelane_b32 v253, s29, 56
	s_add_i32 s14, s15, -1
	v_writelane_b32 v253, s44, 57
	s_cmp_lt_i32 s15, 1
	v_readfirstlane_b32 s0, v0
	v_writelane_b32 v253, s45, 58
	s_cbranch_scc1 .LBB0_65
	s_ashr_i32 s0, s0, 6
	s_min_i32 s18, s0, s14
	s_cmpk_gt_i32 s27, 0x7ff
	v_readlane_b32 s0, v253, 26
	s_cselect_b64 s[20:21], -1, 0
	s_add_u32 s0, s0, 0x800000
	v_writelane_b32 v253, s0, 59
	v_mov_b32_e32 v133, 0
	v_readlane_b32 s0, v253, 27
	s_addc_u32 s0, s0, 0
	s_add_i32 s25, 0, 0x21000
	v_writelane_b32 v253, s0, 61
	s_add_i32 s0, 0, 0x21200
	v_writelane_b32 v253, s0, 63
	s_add_i32 s0, 0, 0x21100
	v_writelane_b32 v254, s0, 1
	s_add_i32 s0, 0, 0x21300
	v_writelane_b32 v254, s0, 3
	v_writelane_b32 v254, s27, 5
	v_writelane_b32 v254, s14, 7
	v_writelane_b32 v254, s15, 9
	v_writelane_b32 v254, s18, 11
	v_writelane_b32 v254, s20, 13
	s_mov_b32 s22, 0x42800000
	s_mov_b32 s19, 0
	v_writelane_b32 v254, s21, 14
	s_branch .LBB0_45

.LBB0_297:
	s_waitcnt vmcnt(0)
	v_readlane_b32 s37, v253, 9
	s_barrier
	v_readlane_b32 s27, v253, 8
	s_cmpk_lg_i32 s37, 0x100
	s_cbranch_scc1 .Lfill_done
	s_cmpk_lt_i32 s27, 0x80
	s_cbranch_scc1 .Lfill_done
	v_readfirstlane_b32 s1, v0
	s_lshl_b32 s0, s27, 3
	s_lshr_b32 s1, s1, 6
	s_add_i32 s0, s0, s1
	s_lshl_b32 s1, s36, 10
	s_add_i32 s0, s0, s1
	s_addk_i32 s0, 0x3400
	v_readlane_b32 s62, v253, 54
	v_readlane_b32 s26, v253, 55
	v_mov_b32_e32 v135, v0
	v_and_b32_e32 v132, 63, v0
	s_mul_hi_i32 s1, s0, 0x3e0f83e1
	s_lshr_b32 s2, s1, 31
	s_ashr_i32 s6, s1, 11
	s_add_i32 s6, s6, s2
	s_mul_i32 s1, s6, 0x2100
	s_sub_i32 s12, s0, s1
	s_mul_i32 s1, s6, 0x11400000
	s_mul_hi_i32 s0, s6, 0x11400000
	s_add_u32 s1, s62, s1
	s_addc_u32 s0, s26, s0
	s_add_u32 s10, s1, 0x800000
	s_addc_u32 s11, s0, 0
	v_lshlrev_b32_e32 v136, 2, v132
	v_lshrrev_b32_e32 v2, 4, v135
	s_mov_b64 s[0:1], -1
	s_cmpk_gt_i32 s12, 0x15ff
	v_and_b32_e32 v133, 7, v135
	v_and_b32_e32 v137, 0x7c, v136
	v_and_b32_e32 v134, 2, v2
	s_cbranch_scc0 .Lfill_done
	s_add_i32 s0, s12, 0xffffea00
	s_mul_i32 s1, s0, 0xba2f
	s_lshr_b32 s3, s1, 23
	s_mul_i32 s1, s3, 0xffffff50
	s_add_i32 s1, s1, s0
	s_lshl_b32 s0, s1, 4
	s_and_b32 s2, s0, 0xffffff80
	s_lshl_b32 s0, s6, 4
	s_add_i32 s0, s0, s3
	s_mul_hi_i32 s1, s0, 0xb00
	s_mulk_i32 s0, 0xb00
	s_ashr_i32 s4, s2, 31
	s_add_u32 s0, s0, s2
	s_addc_u32 s1, s1, s4
	v_readlane_b32 s16, v253, 40
	s_lshl_b64 s[0:1], s[0:1], 12
	v_readlane_b32 s24, v253, 48
	v_readlane_b32 s25, v253, 49
	s_add_u32 s0, s24, s0
	s_addc_u32 s1, s25, s1
	s_lshl_b32 s5, s12, 7
	s_and_b32 s5, s5, 0x380
	s_lshl_b32 s7, s5, 2
	s_add_u32 s0, s0, s7
	s_addc_u32 s1, s1, 0
	v_lshlrev_b32_e32 v194, 2, v137
	v_readlane_b32 s18, v253, 42
	v_lshl_add_u64 v[2:3], s[0:1], 0, v[194:195]
	v_readlane_b32 s0, v253, 56
	v_lshlrev_b32_e32 v4, 12, v135
	v_and_b32_e32 v139, 0x20000, v4
	v_lshl_add_u32 v138, v137, 7, s0
	s_mov_b32 s7, 0
	s_mov_b64 s[0:1], -1
	s_mov_b32 s9, 0x8000
	s_mov_b32 s13, 0x16000
	s_mov_b32 s14, 0x18000
	s_mov_b32 s15, 0x1e000
	s_mov_b32 s16, 0xc000
	s_mov_b32 s18, 0x42800000
	v_readlane_b32 s17, v253, 41
	v_readlane_b32 s19, v253, 43
	v_readlane_b32 s20, v253, 44
	v_readlane_b32 s21, v253, 45
	v_readlane_b32 s22, v253, 46
	v_readlane_b32 s23, v253, 47
	v_readlane_b32 s26, v253, 50
	v_readlane_b32 s27, v253, 51
	v_readlane_b32 s28, v253, 52
	v_readlane_b32 s29, v253, 53
	v_readlane_b32 s30, v253, 54
	v_readlane_b32 s31, v253, 55

.Lfill_done:
.LBB0_298:
	s_getreg_b32 s0, hwreg(HW_REG_XCC_ID, 0, 4)
	s_waitcnt vmcnt(0)
	s_waitcnt vmcnt(0) lgkmcnt(0)
	s_barrier
	s_mov_b64 s[2:3], exec
	v_readlane_b32 s4, v253, 4
	v_readlane_b32 s5, v253, 5
	s_and_b64 s[4:5], s[2:3], s[4:5]
	s_xor_b64 s[30:31], s[4:5], s[2:3]
	s_mov_b64 exec, s[4:5]
	s_cbranch_execz .LBB0_352
	v_readlane_b32 s1, v254, 24
	s_waitcnt vmcnt(0) expcnt(0) lgkmcnt(0)
	s_and_b32 s37, s0, 15
	v_mov_b32_e32 v2, s1
	ds_read_b32 v4, v2
	v_readlane_b32 s1, v254, 17
	s_waitcnt lgkmcnt(0)
	v_cmp_ne_u32_e32 vcc, 0, v4
	v_mov_b32_e32 v2, s1
	ds_read_b32 v2, v2
	s_cbranch_vccnz .LBB0_315
	v_readlane_b32 s2, v253, 0
	v_readlane_b32 s3, v253, 1
	s_load_dwordx2 s[0:1], s[2:3], 0x4
	v_readlane_b32 s2, v253, 9
	s_mov_b32 s16, 1
	s_waitcnt lgkmcnt(0)
	s_mul_i32 s17, s0, s2
	s_mul_i32 s17, s17, s1
	s_mov_b64 s[0:1], 0
	s_branch .LBB0_303
